# combine pass: defer first-row h unpack so expert-row loads issue before the drain (on top of nt weight stores + fp8 first-tile prefetch)
# speedup vs baseline: 1.0005x; 1.0005x over previous
; __device__ __forceinline__ void combine_pass(CTXA, int layer) {
;     ...
;     const float* g = INP(4) + layer * D;
;     f32x4 gv[4];
; #pragma unroll
;     for (int j = 0; j < 4; ++j) gv[j] = *(const f32x4*)(g + 4 * F.lane + 256 * j);
;     const int vcu = F.gw / NWAVES, ntrip = ((T / 64 - vcu + F.G - 1) / F.G) * 4;
;     ...
;     int sln[2];
; #pragma unroll
;     for (int rr = 0; rr < 2; ++rr) { const int row = CMB_ROW(0, rr); sln[rr] = (ntrip > 0) ? SLOTOF[((size_t)((row >> 12) * NE + (F.lane & 15))) * S + (row & 4095)] : -1; }
.LBB0_52:
	s_abs_i32 s7, s34
	v_cvt_f32_u32_e32 v2, s7
	s_lshl_b32 s2, s2, 3
	s_ashr_i32 s8, s1, 6
	s_add_i32 s1, s2, s8
	v_rcp_iflag_f32_e32 v2, v2
	s_ashr_i32 s2, s1, 31
	s_lshr_b32 s2, s2, 29
	s_add_i32 s1, s1, s2
	v_mul_f32_e32 v2, 0x4f7ffffe, v2
	v_cvt_u32_f32_e32 v2, v2
	s_ashr_i32 s1, s1, 3
	s_sub_i32 s12, 0, s7
	s_sub_i32 s2, s34, s1
	v_readfirstlane_b32 s13, v2
	s_mul_i32 s12, s12, s13
	s_addk_i32 s2, 0xff
	s_mul_hi_u32 s12, s13, s12
	s_xor_b32 s9, s2, s34
	s_abs_i32 s2, s2
	s_add_i32 s13, s13, s12
	s_mul_hi_u32 s12, s2, s13
	s_mul_i32 s13, s12, s7
	s_sub_i32 s2, s2, s13
	s_ashr_i32 s9, s9, 31
	s_add_i32 s13, s12, 1
	s_sub_i32 s14, s2, s7
	s_cmp_ge_u32 s2, s7
	s_cselect_b32 s12, s13, s12
	s_cselect_b32 s2, s14, s2
	s_add_i32 s13, s12, 1
	s_cmp_ge_u32 s2, s7
	s_cselect_b32 s2, s13, s12
	s_xor_b32 s2, s2, s9
	s_sub_i32 s9, s2, s9
	s_cmp_lt_i32 s9, 1
	s_cbranch_scc1 .LBB0_66
	v_readlane_b32 s12, v254, 51
	s_ashr_i32 s7, s6, 31
	v_readlane_b32 s14, v254, 53
	v_readlane_b32 s13, v254, 52
	v_readlane_b32 s15, v254, 54
	s_add_u32 s12, s14, s6
	s_addc_u32 s13, s15, s7
	s_lshl_b64 s[6:7], s[6:7], 3
	v_readlane_b32 s14, v253, 0
	v_readlane_b32 s15, v253, 1
	s_add_u32 s6, s14, s6
	s_addc_u32 s7, s15, s7
	s_load_dwordx2 s[6:7], s[6:7], 0x20
	s_lshl_b32 s2, s44, 10
	s_lshl_b64 s[14:15], s[2:3], 2
	v_lshlrev_b32_e32 v2, 2, v1
	v_and_b32_e32 v66, 0xfc, v2
	s_waitcnt lgkmcnt(0)
	s_add_u32 s6, s6, s14
	s_addc_u32 s7, s7, s15
	s_add_u32 s16, s12, 0x36b00000
	s_addc_u32 s17, s13, 0
	s_lshl_b32 s20, s8, 3
	s_lshl_b32 s2, s1, 6
	v_lshlrev_b32_e32 v14, 2, v66
	s_add_i32 s2, s2, s20
	global_load_dwordx4 v[2:5], v14, s[6:7]
	global_load_dwordx4 v[6:9], v14, s[6:7] offset:1024
	global_load_dwordx4 v[10:13], v14, s[6:7] offset:2048
	s_nop 0
	global_load_dwordx4 v[14:17], v14, s[6:7] offset:3072
	s_ashr_i32 s6, s2, 8
	v_bfi_b32 v18, -16, s6, v1
	v_ashrrev_i32_e32 v19, 31, v18
	v_lshlrev_b64 v[18:19], 14, v[18:19]
	s_and_b32 s2, s2, 0xff8
	v_lshl_add_u64 v[18:19], s[16:17], 0, v[18:19]
	s_lshl_b32 s2, s2, 2
	v_lshl_add_u64 v[18:19], v[18:19], 0, s[2:3]
	global_load_dwordx2 v[24:25], v[18:19], off
	v_lshlrev_b32_e32 v18, 1, v66
	v_mov_b32_e32 v19, v67
	v_lshl_add_u64 v[18:19], s[12:13], 0, v[18:19]
	s_mov_b64 s[6:7], 0x4ec00000
	v_lshl_add_u64 v[18:19], v[18:19], 0, s[6:7]
	v_lshl_add_u64 v[22:23], s[12:13], 0, v[66:67]
	s_mov_b64 s[6:7], 0x42c00000
	s_lshl_b32 s21, s9, 2
	v_lshl_add_u64 v[20:21], v[22:23], 0, s[6:7]
	s_mov_b64 s[6:7], 0x24400000
	v_and_b32_e32 v1, 15, v1
	v_lshl_add_u64 v[22:23], v[22:23], 0, s[6:7]
	s_max_i32 s24, s21, 1
	s_mov_b32 s9, 0
	s_waitcnt vmcnt(0)
	s_branch .LBB0_56

; __device__ __forceinline__ unsigned cvt_pk_bf16(float lo, float hi) { unsigned r; asm("v_cvt_pk_bf16_f32 %0, %1, %2" : "=v"(r) : "v"(lo), "v"(hi)); return r; }
; __device__ __forceinline__ unsigned pk4_fp8(float a, float b, float c, float d) { int w = 0; w = __builtin_amdgcn_cvt_pk_fp8_f32(a, b, w, false); w = __builtin_amdgcn_cvt_pk_fp8_f32(c, d, w, true); return (unsigned)w; }
; __device__ __forceinline__ float clamp448(float x) { return __builtin_amdgcn_fmed3f(x, -448.f, 448.f); }
; __device__ __forceinline__ void combine_pass(CTXA, int layer) {
;     ...
;             float ss = 0.f;
; #pragma unroll
;             for (int j = 0; j < 4; ++j) { u32x2 hw2; hw2.x = cvt_pk_bf16(v[rr][j][0], v[rr][j][1]); hw2.y = cvt_pk_bf16(v[rr][j][2], v[rr][j][3]); *(u32x2*)(H + (size_t)row * D + 4 * F.lane + 256 * j) = hw2; ss += (v[rr][j][0] * v[rr][j][0] + v[rr][j][1] * v[rr][j][1]) + (v[rr][j][2] * v[rr][j][2] + v[rr][j][3] * v[rr][j][3]); }
;             const float rs = rsqrtf(wave_sum(ss) * (1.f / D) + EPS);
; #pragma unroll
;             for (int j = 0; j < 4; ++j) { const f32x4 o = v[rr][j] * rs * gv[j]; *(unsigned*)(XN8 + (size_t)row * D + 4 * F.lane + 256 * j) = pk4_fp8(clamp448(8.f * o[0]), clamp448(8.f * o[1]), clamp448(8.f * o[2]), clamp448(8.f * o[3])); } }
.LBB0_55:
	v_cvt_pk_bf16_f32 v24, v40, v41
	v_cvt_pk_bf16_f32 v25, v42, v43
	global_store_dwordx2 v[138:139], v[24:25], off
	v_pk_mul_f32 v[24:25], v[42:43], v[42:43]
	v_pk_mul_f32 v[48:49], v[40:41], v[40:41]
	v_mul_f32_e32 v44, v29, v29
	v_pk_mov_b32 v[52:53], v[48:49], v[24:25] op_sel:[1,0]
	v_mov_b32_e32 v49, v25
	v_pk_add_f32 v[24:25], v[52:53], v[48:49]
	v_cvt_pk_bf16_f32 v48, v36, v37
	v_cvt_pk_bf16_f32 v49, v38, v39
	global_store_dwordx2 v[138:139], v[48:49], off offset:512
	v_pk_mul_f32 v[48:49], v[38:39], v[38:39]
	v_pk_mul_f32 v[52:53], v[36:37], v[36:37]
	v_pk_add_f32 v[24:25], v[24:25], v[24:25] op_sel:[0,1] op_sel_hi:[1,0]
	v_pk_mov_b32 v[54:55], v[52:53], v[48:49] op_sel:[1,0]
	v_mov_b32_e32 v53, v49
	v_pk_add_f32 v[48:49], v[54:55], v[52:53]
	v_cvt_pk_bf16_f32 v52, v32, v33
	v_cvt_pk_bf16_f32 v53, v34, v35
	global_store_dwordx2 v[138:139], v[52:53], off offset:1024
	v_cvt_pk_bf16_f32 v52, v28, v29
	v_cvt_pk_bf16_f32 v53, v30, v31
	global_store_dwordx2 v[138:139], v[52:53], off offset:1536
	v_mul_f32_e32 v26, v28, v28
	v_mov_b32_e32 v25, v26
	v_pk_add_f32 v[26:27], v[48:49], v[48:49] op_sel:[0,1] op_sel_hi:[1,0]
	v_mul_f32_e32 v46, v30, v30
	v_mov_b32_e32 v27, v44
	v_pk_add_f32 v[24:25], v[24:25], v[26:27]
	v_mul_f32_e32 v26, v33, v33
	v_mul_f32_e32 v44, v35, v35
	v_mul_f32_e32 v50, v31, v31
	v_pk_fma_f32 v[26:27], v[32:33], v[32:33], v[26:27] op_sel_hi:[1,1,0]
	v_pk_fma_f32 v[48:49], v[34:35], v[34:35], v[44:45] op_sel_hi:[1,1,0]
	v_mov_b32_e32 v27, v46
	v_mov_b32_e32 v49, v50
	v_pk_add_f32 v[26:27], v[26:27], v[48:49]
	s_lshl_b64 s[6:7], s[36:37], 10
	v_pk_add_f32 v[24:25], v[24:25], v[26:27]
	v_lshl_add_u64 v[26:27], v[22:23], 0, s[6:7]
	v_add_f32_e32 v24, v24, v25
	ds_bpermute_b32 v25, v45, v24
	s_cmp_eq_u32 s25, s24
	s_mov_b32 s9, s25
	s_waitcnt lgkmcnt(0)
	v_add_f32_e32 v24, v24, v25
	ds_bpermute_b32 v25, v47, v24
	s_waitcnt lgkmcnt(0)
	v_add_f32_e32 v24, v24, v25
	ds_bpermute_b32 v25, v51, v24
	s_waitcnt lgkmcnt(0)
	v_add_f32_e32 v24, v24, v25
	ds_bpermute_b32 v25, v87, v24
	s_waitcnt lgkmcnt(0)
	v_add_f32_e32 v24, v24, v25
	ds_bpermute_b32 v25, v88, v24
	s_waitcnt lgkmcnt(0)
	v_add_f32_e32 v24, v24, v25
	ds_bpermute_b32 v25, v89, v24
	s_waitcnt lgkmcnt(0)
	v_add_f32_e32 v24, v24, v25
	v_fmamk_f32 v24, v24, 0x3a800000, v196
	v_cmp_gt_f32_e32 vcc, s39, v24
	v_mul_f32_e32 v25, 0x4b800000, v24
	s_nop 0
	v_cndmask_b32_e32 v24, v24, v25, vcc
	v_rsq_f32_e32 v24, v24
	s_nop 0
	v_mul_f32_e32 v25, 0x45800000, v24
	v_cndmask_b32_e32 v24, v24, v25, vcc
	v_pk_mul_f32 v[40:41], v[40:41], v[24:25] op_sel_hi:[1,0]
	v_pk_mul_f32 v[42:43], v[42:43], v[24:25] op_sel_hi:[1,0]
	v_pk_mul_f32 v[40:41], v[2:3], v[40:41]
	v_pk_mul_f32 v[42:43], v[4:5], v[42:43]
	v_mul_f32_e32 v25, 0x41000000, v40
	v_med3_f32 v25, v25, s19, v248
	v_mul_f32_e32 v40, 0x41000000, v41
	v_pk_mul_f32 v[36:37], v[36:37], v[24:25] op_sel_hi:[1,0]
	v_med3_f32 v40, v40, s19, v248
	v_mul_f32_e32 v41, 0x41000000, v42
	v_mul_f32_e32 v42, 0x41000000, v43
	v_mov_b32_e32 v43, v67
	v_pk_mul_f32 v[36:37], v[6:7], v[36:37]
	v_cvt_pk_fp8_f32 v43, v25, v40
	v_pk_mul_f32 v[38:39], v[38:39], v[24:25] op_sel_hi:[1,0]
	v_mul_f32_e32 v25, 0x41000000, v36
	v_med3_f32 v25, v25, s19, v248
	v_pk_mul_f32 v[38:39], v[8:9], v[38:39]
	v_mul_f32_e32 v36, 0x41000000, v37
	v_pk_mul_f32 v[32:33], v[32:33], v[24:25] op_sel_hi:[1,0]
	v_med3_f32 v36, v36, s19, v248
	v_mul_f32_e32 v37, 0x41000000, v38
	v_mul_f32_e32 v38, 0x41000000, v39
	v_mov_b32_e32 v39, v67
	v_pk_mul_f32 v[32:33], v[10:11], v[32:33]
	v_cvt_pk_fp8_f32 v39, v25, v36
	v_pk_mul_f32 v[34:35], v[34:35], v[24:25] op_sel_hi:[1,0]
	v_mul_f32_e32 v25, 0x41000000, v32
	v_med3_f32 v25, v25, s19, v248
	v_pk_mul_f32 v[28:29], v[28:29], v[24:25] op_sel_hi:[1,0]
	v_pk_mul_f32 v[34:35], v[12:13], v[34:35]
	v_mul_f32_e32 v32, 0x41000000, v33
	v_pk_mul_f32 v[28:29], v[14:15], v[28:29]
	v_med3_f32 v32, v32, s19, v248
	v_mul_f32_e32 v33, 0x41000000, v34
	v_mul_f32_e32 v34, 0x41000000, v35
	v_mov_b32_e32 v35, v67
	v_mul_f32_e32 v28, 0x41000000, v28
	v_mul_f32_e32 v29, 0x41000000, v29
	v_cvt_pk_fp8_f32 v35, v25, v32
	v_pk_mul_f32 v[24:25], v[30:31], v[24:25] op_sel_hi:[1,0]
	v_med3_f32 v28, v28, s19, v248
	v_med3_f32 v29, v29, s19, v248
	v_mov_b32_e32 v30, v67
	v_cvt_pk_fp8_f32 v30, v28, v29
	v_pk_mul_f32 v[24:25], v[16:17], v[24:25]
	v_med3_f32 v41, v41, s19, v248
	v_mul_f32_e32 v24, 0x41000000, v24
	v_mul_f32_e32 v25, 0x41000000, v25
	v_med3_f32 v42, v42, s19, v248
	v_med3_f32 v37, v37, s19, v248
	v_med3_f32 v38, v38, s19, v248
	v_med3_f32 v33, v33, s19, v248
	v_med3_f32 v34, v34, s19, v248
	v_med3_f32 v24, v24, s19, v248
	v_med3_f32 v25, v25, s19, v248
	v_cvt_pk_fp8_f32 v43, v41, v42 op_sel:[0,0,1]
	v_cvt_pk_fp8_f32 v39, v37, v38 op_sel:[0,0,1]
	v_cvt_pk_fp8_f32 v35, v33, v34 op_sel:[0,0,1]
	v_cvt_pk_fp8_f32 v30, v24, v25 op_sel:[0,0,1]
	v_mov_b32_e32 v24, v70
	v_mov_b32_e32 v25, v66
	global_store_dword v[26:27], v43, off
	global_store_dword v[26:27], v39, off offset:256
	global_store_dword v[26:27], v35, off offset:512
	global_store_dword v[26:27], v30, off offset:768
	s_cbranch_scc1 .LBB0_66

; __device__ __forceinline__ float bf_lo(unsigned w) { return __uint_as_float(w << 16); }
; __device__ __forceinline__ float bf_hi(unsigned w) { return __uint_as_float(w & 0xffff0000u); }
; __device__ __forceinline__ void combine_pass(CTXA, int layer) {
;     ...
;         for (int rr = 0; rr < 2; ++rr) { const int row = CMB_ROW(tp, rr);
;             sl[rr] = sln[rr]; { const int rown = CMB_ROW(tp + 1, rr); sln[rr] = (tp + 1 < ntrip) ? SLOTOF[((size_t)((rown >> 12) * NE + (F.lane & 15))) * S + (rown & 4095)] : -1; }
; #pragma unroll
;             for (int j = 0; j < 4; ++j) { const u32x2 w = *(const u32x2*)(H + (size_t)row * D + 4 * F.lane + 256 * j); v[rr][j] = (f32x4){bf_lo(w.x), bf_hi(w.x), bf_lo(w.y), bf_hi(w.y)}; } }
; #pragma unroll
;         for (int rr = 0; rr < 2; ++rr) { const int row = CMB_ROW(tp, rr), b = row >> 12;
;             em[rr] = (unsigned)(__ballot(sl[rr] >= 0) & 0xFFFFull);
; #pragma unroll
;             for (int q = 0; q < 4; ++q) { const bool valid = em[rr] != 0u; const int e = valid ? __builtin_ctz(em[rr]) : 0; em[rr] &= em[rr] - 1u;
;                 const int se = __builtin_amdgcn_readlane(sl[rr], e); wgt[rr][q] = __builtin_ldexpf(valid ? 1.f : 0.f, -6);
;                 const unsigned char* y = YG + ((size_t)((e * NB + b) * CAP + (valid ? se : 0))) * D + 4 * F.lane;
; #pragma unroll
;                 for (int j = 0; j < 4; ++j) yw[rr][q][j] = *(const unsigned*)(y + 256 * j); } }
.LBB0_60:
	s_or_b32 s36, s40, 1
	s_ashr_i32 s37, s36, 31
	s_lshl_b64 s[6:7], s[36:37], 11
	v_lshl_add_u64 v[138:139], v[18:19], 0, s[6:7]
	v_cmp_lt_i32_e64 s[6:7], -1, v24
	s_ashr_i32 s2, s8, 3
	s_and_b32 s7, s6, 0xffff
	s_add_i32 s6, s6, -1
	s_and_b32 s2, s2, 0xfffffe00
	s_and_b32 s8, s6, s7
	s_cmp_eq_u32 s7, 0
	s_ff1_i32_b32 s9, s7
	s_cselect_b64 s[6:7], -1, 0
	v_cndmask_b32_e64 v54, v250, 0, s[6:7]
	s_and_b64 s[6:7], s[6:7], exec
	s_cselect_b32 s6, 0, s9
	v_readlane_b32 s7, v24, s6
	s_cselect_b32 s7, 0, s7
	s_lshl_b32 s6, s6, 11
	s_add_i32 s7, s7, s2
	s_add_i32 s6, s7, s6
	s_ashr_i32 s7, s6, 31
	s_lshl_b64 s[6:7], s[6:7], 10
	v_lshl_add_u64 v[58:59], v[20:21], 0, s[6:7]
	s_add_i32 s6, s8, -1
	s_and_b32 s9, s6, s8
	s_cmp_eq_u32 s8, 0
	s_cselect_b64 s[6:7], -1, 0
	s_ff1_i32_b32 s8, s8
	v_cndmask_b32_e64 v56, v250, 0, s[6:7]
	s_and_b64 s[6:7], s[6:7], exec
	s_cselect_b32 s6, 0, s8
	v_readlane_b32 s7, v24, s6
	s_cselect_b32 s7, 0, s7
	s_lshl_b32 s6, s6, 11
	s_add_i32 s6, s6, s2
	s_add_i32 s6, s6, s7
	s_ashr_i32 s7, s6, 31
	s_lshl_b64 s[6:7], s[6:7], 10
	v_lshl_add_u64 v[60:61], v[20:21], 0, s[6:7]
	s_add_i32 s6, s9, -1
	s_and_b32 s8, s6, s9
	s_cmp_eq_u32 s9, 0
	s_cselect_b64 s[6:7], -1, 0
	global_load_dwordx2 v[50:51], v[138:139], off
	global_load_dwordx2 v[48:49], v[138:139], off offset:512
	global_load_dwordx2 v[46:47], v[138:139], off offset:1024
	global_load_dwordx2 v[44:45], v[138:139], off offset:1536
	global_load_dword v55, v[58:59], off
	global_load_dword v57, v[58:59], off offset:256
	global_load_dword v87, v[58:59], off offset:512
	s_nop 0
	global_load_dword v59, v[58:59], off offset:768
	s_nop 0
	global_load_dword v101, v[60:61], off
	global_load_dword v105, v[60:61], off offset:256
	global_load_dword v109, v[60:61], off offset:512
	s_nop 0
	global_load_dword v61, v[60:61], off offset:768
	s_ff1_i32_b32 s9, s9
	v_cndmask_b32_e64 v58, v250, 0, s[6:7]
	s_and_b64 s[6:7], s[6:7], exec
	s_cselect_b32 s6, 0, s9
	v_readlane_b32 s7, v24, s6
	s_cselect_b32 s7, 0, s7
	s_lshl_b32 s6, s6, 11
	s_add_i32 s6, s6, s2
	s_add_i32 s6, s6, s7
	s_ashr_i32 s7, s6, 31
	s_lshl_b64 s[6:7], s[6:7], 10
	v_lshl_add_u64 v[62:63], v[20:21], 0, s[6:7]
	s_add_i32 s6, s8, -1
	s_and_b32 s26, s6, s8
	s_cmp_eq_u32 s8, 0
	s_cselect_b64 s[6:7], -1, 0
	s_ff1_i32_b32 s8, s8
	v_cndmask_b32_e64 v60, v250, 0, s[6:7]
	s_and_b64 s[6:7], s[6:7], exec
	s_cselect_b32 s6, 0, s8
	v_readlane_b32 s7, v24, s6
	s_cselect_b32 s7, 0, s7
	s_lshl_b32 s6, s6, 11
	s_add_i32 s6, s6, s2
	s_add_i32 s6, s6, s7
	s_ashr_i32 s7, s6, 31
	s_lshl_b64 s[6:7], s[6:7], 10
	v_lshl_add_u64 v[64:65], v[20:21], 0, s[6:7]
	v_cmp_lt_i32_e64 s[6:7], -1, v25
	s_and_b32 s8, s6, 0xffff
	s_add_i32 s6, s6, -1
	s_and_b32 s12, s6, s8
	s_cmp_eq_u32 s8, 0
	s_cselect_b64 s[6:7], -1, 0
	s_ff1_i32_b32 s13, s8
	s_and_b64 s[8:9], s[6:7], exec
	s_cselect_b32 s8, 0, s13
	v_readlane_b32 s9, v25, s8
	s_cselect_b32 s9, 0, s9
	s_lshl_b32 s8, s8, 11
	s_add_i32 s9, s9, s2
	s_add_i32 s8, s9, s8
	s_ashr_i32 s9, s8, 31
	s_lshl_b64 s[8:9], s[8:9], 10
	global_load_dword v117, v[62:63], off
	global_load_dword v121, v[62:63], off offset:256
	global_load_dword v125, v[62:63], off offset:512
	global_load_dword v129, v[62:63], off offset:768
	global_load_dword v132, v[64:65], off
	global_load_dword v133, v[64:65], off offset:256
	global_load_dword v134, v[64:65], off offset:512
	global_load_dword v135, v[64:65], off offset:768
	v_lshl_add_u64 v[62:63], v[20:21], 0, s[8:9]
	s_add_i32 s8, s12, -1
	s_and_b32 s14, s8, s12
	s_cmp_eq_u32 s12, 0
	s_cselect_b64 s[8:9], -1, 0
	s_ff1_i32_b32 s15, s12
	s_and_b64 s[12:13], s[8:9], exec
	s_cselect_b32 s12, 0, s15
	v_readlane_b32 s13, v25, s12
	s_cselect_b32 s13, 0, s13
	s_lshl_b32 s12, s12, 11
	s_add_i32 s12, s12, s2
	s_add_i32 s12, s12, s13
	s_ashr_i32 s13, s12, 31
	s_lshl_b64 s[12:13], s[12:13], 10
	v_lshl_add_u64 v[64:65], v[20:21], 0, s[12:13]
	s_add_i32 s12, s14, -1
	s_and_b32 s27, s12, s14
	s_cmp_eq_u32 s14, 0
	s_cselect_b64 s[12:13], -1, 0
	s_ff1_i32_b32 s28, s14
	s_and_b64 s[14:15], s[12:13], exec
	s_cselect_b32 s14, 0, s28
	v_readlane_b32 s15, v25, s14
	s_cselect_b32 s15, 0, s15
	s_lshl_b32 s14, s14, 11
	s_add_i32 s14, s14, s2
	s_add_i32 s14, s14, s15
	s_ashr_i32 s15, s14, 31
	s_lshl_b64 s[14:15], s[14:15], 10
	s_cmp_eq_u32 s27, 0
	global_load_dword v82, v[62:63], off
	global_load_dword v81, v[62:63], off offset:256
	global_load_dword v80, v[62:63], off offset:512
	global_load_dword v79, v[62:63], off offset:768
	global_load_dword v78, v[64:65], off
	global_load_dword v77, v[64:65], off offset:256
	global_load_dword v75, v[64:65], off offset:512
	global_load_dword v74, v[64:65], off offset:768
	v_lshl_add_u64 v[62:63], v[20:21], 0, s[14:15]
	s_cselect_b64 s[14:15], -1, 0
	s_ff1_i32_b32 s30, s27
	s_and_b64 s[28:29], s[14:15], exec
	s_cselect_b32 s28, 0, s30
	v_readlane_b32 s29, v25, s28
	s_cselect_b32 s29, 0, s29
	s_lshl_b32 s28, s28, 11
	s_add_i32 s28, s28, s2
	s_add_i32 s28, s28, s29
	s_ashr_i32 s29, s28, 31
	s_lshl_b64 s[28:29], s[28:29], 10
	v_lshl_add_u64 v[64:65], v[20:21], 0, s[28:29]
	global_load_dword v86, v[62:63], off
	global_load_dword v85, v[62:63], off offset:256
	global_load_dword v84, v[62:63], off offset:512
	global_load_dword v83, v[62:63], off offset:768
	global_load_dword v76, v[64:65], off
	global_load_dword v73, v[64:65], off offset:256
	global_load_dword v72, v[64:65], off offset:512
	global_load_dword v71, v[64:65], off offset:768
	s_waitcnt vmcnt(36)
; __device__ __forceinline__ float bf_lo(unsigned w) { return __uint_as_float(w << 16); }
; __device__ __forceinline__ float bf_hi(unsigned w) { return __uint_as_float(w & 0xffff0000u); }
; __device__ __forceinline__ void combine_pass(CTXA, int layer) {
;     ...
;             for (int j = 0; j < 4; ++j) { const u32x2 w = *(const u32x2*)(H + (size_t)row * D + 4 * F.lane + 256 * j); v[rr][j] = (f32x4){bf_lo(w.x), bf_hi(w.x), bf_lo(w.y), bf_hi(w.y)}; } }
; #pragma unroll
;         for (int rr = 0; rr < 2; ++rr) { const int row = CMB_ROW(tp, rr), b = row >> 12;
;             em[rr] = (unsigned)(__ballot(sl[rr] >= 0) & 0xFFFFull);
; #pragma unroll
;             for (int q = 0; q < 4; ++q) { const bool valid = em[rr] != 0u; const int e = valid ? __builtin_ctz(em[rr]) : 0; em[rr] &= em[rr] - 1u;
;                 const int se = __builtin_amdgcn_readlane(sl[rr], e); wgt[rr][q] = __builtin_ldexpf(valid ? 1.f : 0.f, -6);
;                 const unsigned char* y = YG + ((size_t)((e * NB + b) * CAP + (valid ? se : 0))) * D + 4 * F.lane;
; #pragma unroll
;                 for (int j = 0; j < 4; ++j) yw[rr][q][j] = *(const unsigned*)(y + 256 * j); } }
; #pragma unroll
;         for (int rr = 0; rr < 2; ++rr) { const int row = CMB_ROW(tp, rr), b = row >> 12;
; #pragma unroll
;             for (int q = 0; q < 4; ++q)
; #pragma unroll
;                 for (int j = 0; j < 4; ++j) { const int w = (int)yw[rr][q][j]; const float g1 = wgt[rr][q];
;                     v[rr][j][0] += g1 * __builtin_amdgcn_cvt_f32_fp8(w, 0); v[rr][j][1] += g1 * __builtin_amdgcn_cvt_f32_fp8(w, 1); v[rr][j][2] += g1 * __builtin_amdgcn_cvt_f32_fp8(w, 2); v[rr][j][3] += g1 * __builtin_amdgcn_cvt_f32_fp8(w, 3); }
;             unsigned m2 = em[rr];
	v_lshlrev_b32_e32 v42, 16, v36
	v_and_b32_e32 v43, 0xffff0000, v36
	v_lshlrev_b32_e32 v52, 16, v37
	v_and_b32_e32 v53, 0xffff0000, v37
	v_lshlrev_b32_e32 v38, 16, v34
	v_and_b32_e32 v39, 0xffff0000, v34
	v_lshlrev_b32_e32 v40, 16, v35
	v_and_b32_e32 v41, 0xffff0000, v35
	v_lshlrev_b32_e32 v34, 16, v32
	v_and_b32_e32 v35, 0xffff0000, v32
	v_lshlrev_b32_e32 v36, 16, v33
	v_and_b32_e32 v37, 0xffff0000, v33
	v_lshlrev_b32_e32 v30, 16, v26
	v_and_b32_e32 v31, 0xffff0000, v26
	v_lshlrev_b32_e32 v32, 16, v27
	v_and_b32_e32 v33, 0xffff0000, v27
	s_waitcnt vmcnt(31)
	v_cvt_f32_fp8_e32 v62, v55
	v_cvt_f32_fp8_sdwa v63, v55 src0_sel:BYTE_1
	v_cvt_f32_fp8_sdwa v64, v55 src0_sel:BYTE_2
	v_cvt_f32_fp8_sdwa v65, v55 src0_sel:BYTE_3
	s_waitcnt vmcnt(27)
	v_cvt_f32_fp8_e32 v98, v101
	v_cvt_f32_fp8_sdwa v99, v101 src0_sel:BYTE_1
	v_cvt_f32_fp8_sdwa v100, v101 src0_sel:BYTE_2
	v_cvt_f32_fp8_sdwa v101, v101 src0_sel:BYTE_3
	v_pk_fma_f32 v[42:43], v[54:55], v[62:63], v[42:43] op_sel_hi:[0,1,1]
	v_cvt_f32_fp8_e32 v68, v57
	v_cvt_f32_fp8_sdwa v69, v57 src0_sel:BYTE_1
	v_pk_fma_f32 v[52:53], v[54:55], v[64:65], v[52:53] op_sel_hi:[0,1,1]
	s_waitcnt vmcnt(26)
	v_cvt_f32_fp8_e32 v102, v105
	v_cvt_f32_fp8_sdwa v103, v105 src0_sel:BYTE_1
	v_pk_fma_f32 v[52:53], v[56:57], v[100:101], v[52:53] op_sel_hi:[0,1,1]
	v_cvt_f32_fp8_sdwa v88, v57 src0_sel:BYTE_2
	v_cvt_f32_fp8_sdwa v89, v57 src0_sel:BYTE_3
	v_pk_fma_f32 v[38:39], v[54:55], v[68:69], v[38:39] op_sel_hi:[0,1,1]
	v_cvt_f32_fp8_sdwa v104, v105 src0_sel:BYTE_2
	v_cvt_f32_fp8_sdwa v105, v105 src0_sel:BYTE_3
	v_pk_fma_f32 v[38:39], v[56:57], v[102:103], v[38:39] op_sel_hi:[0,1,1]
	v_cvt_f32_fp8_e32 v90, v87
	v_cvt_f32_fp8_sdwa v91, v87 src0_sel:BYTE_1
	v_pk_fma_f32 v[40:41], v[54:55], v[88:89], v[40:41] op_sel_hi:[0,1,1]
	s_waitcnt vmcnt(25)
	v_cvt_f32_fp8_e32 v106, v109
	v_cvt_f32_fp8_sdwa v107, v109 src0_sel:BYTE_1
	s_waitcnt vmcnt(23)
	v_cvt_f32_fp8_e32 v114, v117
	v_cvt_f32_fp8_sdwa v115, v117 src0_sel:BYTE_1
	v_cvt_f32_fp8_sdwa v116, v117 src0_sel:BYTE_2
	v_cvt_f32_fp8_sdwa v117, v117 src0_sel:BYTE_3
	s_waitcnt vmcnt(19)
	v_cvt_f32_fp8_sdwa v62, v132 src0_sel:BYTE_2
	v_cvt_f32_fp8_sdwa v63, v132 src0_sel:BYTE_3
	v_cvt_f32_fp8_e32 v118, v121
	v_cvt_f32_fp8_sdwa v119, v121 src0_sel:BYTE_1
	v_pk_fma_f32 v[52:53], v[58:59], v[116:117], v[52:53] op_sel_hi:[0,1,1]
	v_pk_fma_f32 v[52:53], v[60:61], v[62:63], v[52:53] op_sel_hi:[0,1,1]
	s_waitcnt vmcnt(18)
	v_cvt_f32_fp8_e32 v62, v133
	v_cvt_f32_fp8_sdwa v63, v133 src0_sel:BYTE_1
	v_cvt_f32_fp8_sdwa v120, v121 src0_sel:BYTE_2
	v_cvt_f32_fp8_sdwa v121, v121 src0_sel:BYTE_3
	v_pk_fma_f32 v[38:39], v[58:59], v[118:119], v[38:39] op_sel_hi:[0,1,1]
	v_pk_fma_f32 v[38:39], v[60:61], v[62:63], v[38:39] op_sel_hi:[0,1,1]
	v_cvt_f32_fp8_sdwa v62, v133 src0_sel:BYTE_2
	v_cvt_f32_fp8_sdwa v63, v133 src0_sel:BYTE_3
	v_pk_fma_f32 v[40:41], v[56:57], v[104:105], v[40:41] op_sel_hi:[0,1,1]
	v_cvt_f32_fp8_e32 v122, v125
	v_cvt_f32_fp8_sdwa v123, v125 src0_sel:BYTE_1
	v_pk_fma_f32 v[40:41], v[58:59], v[120:121], v[40:41] op_sel_hi:[0,1,1]
	v_pk_fma_f32 v[40:41], v[60:61], v[62:63], v[40:41] op_sel_hi:[0,1,1]
	s_waitcnt vmcnt(17)
	v_cvt_f32_fp8_e32 v62, v134
	v_cvt_f32_fp8_sdwa v63, v134 src0_sel:BYTE_1
	v_cvt_f32_fp8_sdwa v92, v87 src0_sel:BYTE_2
	v_cvt_f32_fp8_sdwa v93, v87 src0_sel:BYTE_3
	v_pk_fma_f32 v[34:35], v[54:55], v[90:91], v[34:35] op_sel_hi:[0,1,1]
	v_cvt_f32_fp8_sdwa v108, v109 src0_sel:BYTE_2
	v_cvt_f32_fp8_sdwa v109, v109 src0_sel:BYTE_3
	v_pk_fma_f32 v[34:35], v[56:57], v[106:107], v[34:35] op_sel_hi:[0,1,1]
	v_cvt_f32_fp8_sdwa v124, v125 src0_sel:BYTE_2
	v_cvt_f32_fp8_sdwa v125, v125 src0_sel:BYTE_3
	v_pk_fma_f32 v[34:35], v[58:59], v[122:123], v[34:35] op_sel_hi:[0,1,1]
	v_pk_fma_f32 v[34:35], v[60:61], v[62:63], v[34:35] op_sel_hi:[0,1,1]
	v_cvt_f32_fp8_sdwa v62, v134 src0_sel:BYTE_2
	v_cvt_f32_fp8_sdwa v63, v134 src0_sel:BYTE_3
	v_cvt_f32_fp8_e32 v94, v59
	v_cvt_f32_fp8_sdwa v95, v59 src0_sel:BYTE_1
	v_pk_fma_f32 v[36:37], v[54:55], v[92:93], v[36:37] op_sel_hi:[0,1,1]
	v_cvt_f32_fp8_e32 v110, v61
	v_cvt_f32_fp8_sdwa v111, v61 src0_sel:BYTE_1
	v_pk_fma_f32 v[36:37], v[56:57], v[108:109], v[36:37] op_sel_hi:[0,1,1]
	v_cvt_f32_fp8_e32 v126, v129
	v_cvt_f32_fp8_sdwa v127, v129 src0_sel:BYTE_1
	v_pk_fma_f32 v[36:37], v[58:59], v[124:125], v[36:37] op_sel_hi:[0,1,1]
	v_pk_fma_f32 v[36:37], v[60:61], v[62:63], v[36:37] op_sel_hi:[0,1,1]
	s_waitcnt vmcnt(16)
	v_cvt_f32_fp8_e32 v62, v135
	v_cvt_f32_fp8_sdwa v63, v135 src0_sel:BYTE_1
	v_cvt_f32_fp8_sdwa v96, v59 src0_sel:BYTE_2
	v_cvt_f32_fp8_sdwa v97, v59 src0_sel:BYTE_3
	v_pk_fma_f32 v[30:31], v[54:55], v[94:95], v[30:31] op_sel_hi:[0,1,1]
	v_cvt_f32_fp8_sdwa v112, v61 src0_sel:BYTE_2
	v_cvt_f32_fp8_sdwa v113, v61 src0_sel:BYTE_3
	v_pk_fma_f32 v[30:31], v[56:57], v[110:111], v[30:31] op_sel_hi:[0,1,1]
	v_cvt_f32_fp8_sdwa v128, v129 src0_sel:BYTE_2
	v_cvt_f32_fp8_sdwa v129, v129 src0_sel:BYTE_3
	v_pk_fma_f32 v[30:31], v[58:59], v[126:127], v[30:31] op_sel_hi:[0,1,1]
	v_cvt_f32_fp8_e32 v130, v132
	v_cvt_f32_fp8_sdwa v131, v132 src0_sel:BYTE_1
	v_pk_fma_f32 v[30:31], v[60:61], v[62:63], v[30:31] op_sel_hi:[0,1,1]
	v_cvt_f32_fp8_sdwa v62, v135 src0_sel:BYTE_2
	v_cvt_f32_fp8_sdwa v63, v135 src0_sel:BYTE_3
	v_pk_fma_f32 v[32:33], v[54:55], v[96:97], v[32:33] op_sel_hi:[0,1,1]
	v_pk_fma_f32 v[42:43], v[56:57], v[98:99], v[42:43] op_sel_hi:[0,1,1]
	v_pk_fma_f32 v[32:33], v[56:57], v[112:113], v[32:33] op_sel_hi:[0,1,1]
	v_pk_fma_f32 v[42:43], v[58:59], v[114:115], v[42:43] op_sel_hi:[0,1,1]
	v_pk_fma_f32 v[32:33], v[58:59], v[128:129], v[32:33] op_sel_hi:[0,1,1]
	v_pk_fma_f32 v[42:43], v[60:61], v[130:131], v[42:43] op_sel_hi:[0,1,1]
	s_cmp_eq_u32 s26, 0
	v_pk_fma_f32 v[32:33], v[60:61], v[62:63], v[32:33] op_sel_hi:[0,1,1]
	s_cbranch_scc1 .LBB0_62
